# WATT tile ring: A-set hand-over waits vmcnt(2) instead of vmcnt(0) so the B-set loads stay in flight
# speedup vs baseline: 1.0006x; 1.0006x over previous
; #define LAS __attribute__((address_space(3)))
; template <int DK16, int DV32, bool MASK, int HALFWIN, bool RES, bool WT, class P>
; __device__ __forceinline__ void attn_unit(LAS unsigned char* lds, const P& c, const int ntiles, const float C, const int wv) {
;     ...
;             if (do0) {
; #pragma unroll
;                 for (int d0 = 0; d0 < DK16; ++d0) { const bf16x8 b0 = *(const LAS bf16x8*)(Ks + ATT_KSWZ(r32, (d0 * 16 + hi * 8) * 2)); p0 = __builtin_amdgcn_mfma_f32_32x32x16_bf16(b0, qr[d0], p0, 0, 0, 0); } }
;             if (do1) {
; #pragma unroll
;                 for (int d0 = 0; d0 < DK16; ++d0) { const bf16x8 b1 = *(const LAS bf16x8*)(Ks + ATT_KSWZ(32 + r32, (d0 * 16 + hi * 8) * 2)); p1 = __builtin_amdgcn_mfma_f32_32x32x16_bf16(b1, qr[d0], p1, 0, 0, 0); } }
;             if constexpr (MASK) {
;                 const int db = c.dbase(wid, r32, t) + 4 * hi, qi = c.qidx(wid, r32); const unsigned L = (unsigned)c.seqlen(); const bool edge = c.edge();
;                 const LAS float* tb = c.tab(wid) + (db + 2 * HALFWIN);
;     ...
;             if (do0) { bf16x8 pa0, pa1; ATT_PK4(p0, 0, pa0); ATT_PK4(p0, 8, pa1);
;                 pv_half2<0, 1, 0>(o[0], o[1], vb, pa0, pa1);
;                 if constexpr (DV32 == 4) { pv_half2<2, 3, 0>(o[2], o[3], vb, pa0, pa1); } }
;             if (do1) { bf16x8 pa2, pa3; ATT_PK4(p1, 0, pa2); ATT_PK4(p1, 8, pa3);
;                 pv_half2<0, 1, 1>(o[0], o[1], vb, pa2, pa3);
;                 if constexpr (DV32 == 4) { pv_half2<2, 3, 1>(o[2], o[3], vb, pa2, pa3); } }
;     ...
;         }
;     };
;     if constexpr (RES) {
;         ATT_LOAD(A, 0); ATT_LOAD(B, 1); ATT_WRITE(A, 0); ATT_LOAD(A, 2); ATT_WRITE(B, 1); ATT_LOAD(B, 3); ATT_WRITE(A, 2); ATT_WRITE(B, 3);
;         __syncthreads();
;         compute(0, 0); compute(1, 1); compute(2, 2); compute(3, 3);
;         __syncthreads();
;     } else {
;     const int tl = ntiles - 1;
;     ATT_LOAD(A, 0); ATT_WRITE(A, 0); ATT_LOAD(A, (1 < tl ? 1 : tl)); ATT_LOAD(B, (2 < tl ? 2 : tl));
;     __syncthreads();
;     for (int t = 0; t < ntiles; t += 2) {
;         compute(t, 0); ATT_WRITE(A, 1); ATT_LOAD(A, (t + 3 < tl ? t + 3 : tl));
;         __syncthreads();
;         if (t + 1 >= ntiles) break;
;         compute(t + 1, 1); ATT_WRITE(B, 0); ATT_LOAD(B, (t + 4 < tl ? t + 4 : tl));
.LBB0_664:
	v_add_f32_e32 v155, v17, v18
	v_fmac_f32_e32 v155, v158, v16
	v_cvt_pk_bf16_f32 v16, v64, v122
	v_cvt_pk_bf16_f32 v17, v78, v79
	v_cvt_pk_bf16_f32 v18, v76, v77
	v_cvt_pk_bf16_f32 v19, v74, v75
	v_cvt_pk_bf16_f32 v20, v72, v73
	v_cvt_pk_bf16_f32 v21, v70, v71
	v_cvt_pk_bf16_f32 v22, v68, v69
	v_cvt_pk_bf16_f32 v23, v66, v67
	ds_read_b64_tr_b16 v[24:25], v143 offset:0
	ds_read_b64_tr_b16 v[26:27], v143 offset:0x800
	ds_read_b64_tr_b16 v[28:29], v143 offset:0x1000
	ds_read_b64_tr_b16 v[30:31], v143 offset:0x1800
	ds_read_b64_tr_b16 v[66:67], v143 offset:0x200
	ds_read_b64_tr_b16 v[68:69], v143 offset:0xa00
	ds_read_b64_tr_b16 v[70:71], v143 offset:0x1200
	ds_read_b64_tr_b16 v[72:73], v143 offset:0x1a00
	s_waitcnt lgkmcnt(0)
	s_nop 0
	v_permlane32_swap_b32_e32 v16, v18
	v_permlane32_swap_b32_e32 v17, v19
	v_permlane32_swap_b32_e32 v20, v22
	v_permlane32_swap_b32_e32 v21, v23
	v_mfma_f32_32x32x16_bf16 v[48:63], v[16:19], v[66:69], v[48:63]
	v_mfma_f32_32x32x16_bf16 v[32:47], v[16:19], v[24:27], v[32:47]
	v_cvt_pk_bf16_f32 v16, v0, v1
	v_cvt_pk_bf16_f32 v17, v2, v4
	v_cvt_pk_bf16_f32 v18, v8, v12
	v_cvt_pk_bf16_f32 v19, v7, v11
	v_cvt_pk_bf16_f32 v66, v3, v5
	v_cvt_pk_bf16_f32 v67, v6, v10
	v_cvt_pk_bf16_f32 v68, v9, v13
	v_cvt_pk_bf16_f32 v69, v14, v15
	ds_read_b64_tr_b16 v[0:1], v143 offset:0x2000
	ds_read_b64_tr_b16 v[2:3], v143 offset:0x2800
	ds_read_b64_tr_b16 v[4:5], v143 offset:0x3000
	ds_read_b64_tr_b16 v[6:7], v143 offset:0x3800
	ds_read_b64_tr_b16 v[8:9], v143 offset:0x2200
	ds_read_b64_tr_b16 v[10:11], v143 offset:0x2a00
	v_mfma_f32_32x32x16_bf16 v[48:63], v[20:23], v[70:73], v[48:63]
	ds_read_b64_tr_b16 v[70:71], v143 offset:0x3200
	ds_read_b64_tr_b16 v[72:73], v143 offset:0x3a00
	s_waitcnt lgkmcnt(0)
	v_permlane32_swap_b32_e32 v16, v18
	v_permlane32_swap_b32_e32 v17, v19
	v_mfma_f32_32x32x16_bf16 v[32:47], v[20:23], v[28:31], v[32:47]
	v_permlane32_swap_b32_e32 v66, v68
	v_permlane32_swap_b32_e32 v67, v69
	v_mfma_f32_32x32x16_bf16 v[32:47], v[16:19], v[0:3], v[32:47]
	s_cmp_eq_u32 s28, 0
	s_cselect_b32 s18, 0xc0, s70
	s_waitcnt vmcnt(2)
	ds_write_b128 v144, v[108:111] offset:16384
	ds_write_b128 v145, v[104:107] offset:49152
	s_cmpk_eq_i32 s28, 0x400
	v_mfma_f32_32x32x16_bf16 v[48:63], v[16:19], v[8:11], v[48:63]
	s_nop 4
	v_mov_b64_e32 v[16:17], v[32:33]
	v_mov_b64_e32 v[18:19], v[34:35]
	v_mov_b64_e32 v[20:21], v[36:37]
	v_mov_b64_e32 v[22:23], v[38:39]
	v_mov_b64_e32 v[24:25], v[40:41]
	v_mov_b64_e32 v[26:27], v[42:43]
	v_mov_b64_e32 v[28:29], v[44:45]
	v_mov_b64_e32 v[30:31], v[46:47]
	v_add_u32_e32 v32, s18, v142
	v_med3_i32 v32, v32, 0, v221
	v_mul_u32_u24_e32 v64, 0xe00, v32
	v_lshl_add_u64 v[32:33], v[120:121], 0, v[64:65]
	global_load_dwordx4 v[104:107], v[32:33], off offset:3072
	global_load_dwordx4 v[108:111], v[32:33], off offset:3328
	v_mfma_f32_32x32x16_bf16 v[16:31], v[66:69], v[4:7], v[16:31]
	v_mov_b64_e32 v[0:1], v[48:49]
	v_mov_b64_e32 v[2:3], v[50:51]
	v_mov_b64_e32 v[4:5], v[52:53]
	v_mov_b64_e32 v[6:7], v[54:55]
	v_mov_b64_e32 v[8:9], v[56:57]
	v_mov_b64_e32 v[10:11], v[58:59]
	v_mov_b64_e32 v[12:13], v[60:61]
	v_mov_b64_e32 v[14:15], v[62:63]
	s_waitcnt lgkmcnt(0)
	s_barrier
	v_mfma_f32_32x32x16_bf16 v[0:15], v[66:69], v[70:73], v[0:15]
	s_cbranch_scc1 .LBB0_651
	ds_read_b128 v[32:35], v150 offset:49152
	ds_read_b128 v[36:39], v150 offset:57344
	v_add_u32_e32 v64, 0x11300, v154
	v_add_u32_e32 v78, 0x11308, v154
	v_add_u32_e32 v79, 0x11320, v154
	s_waitcnt lgkmcnt(1)
	v_mfma_f32_32x32x16_bf16 v[48:63], v[32:35], v[80:83], 0
	ds_read_b128 v[32:35], v151 offset:49152
	ds_read_b128 v[66:69], v151 offset:57344
	v_add_u32_e32 v122, 0x11328, v154
	s_mov_b64 s[18:19], -1
	s_and_b64 vcc, exec, s[10:11]
	s_waitcnt lgkmcnt(1)
	v_mfma_f32_32x32x16_bf16 v[48:63], v[32:35], v[84:87], v[48:63]
	ds_read_b128 v[32:35], v152 offset:49152
	ds_read_b128 v[70:73], v152 offset:57344
	ds_read_b128 v[158:161], v153 offset:49152
	ds_read_b128 v[74:77], v153 offset:57344
	ds_read2_b32 v[138:139], v64 offset1:1
	ds_read2_b32 v[136:137], v78 offset1:1
	ds_read2_b32 v[134:135], v79 offset1:1
	ds_read2_b32 v[132:133], v122 offset1:1
	v_add_u32_e32 v64, 0x11340, v154
	v_add_u32_e32 v78, 0x11348, v154
	v_add_u32_e32 v79, 0x11360, v154
	v_add_u32_e32 v122, 0x11368, v154
	s_waitcnt lgkmcnt(7)
	v_mfma_f32_32x32x16_bf16 v[48:63], v[32:35], v[88:91], v[48:63]
	ds_read2_b32 v[130:131], v64 offset1:1
	ds_read2_b32 v[128:129], v78 offset1:1
	ds_read2_b32 v[126:127], v79 offset1:1
	ds_read2_b32 v[124:125], v122 offset1:1
	s_waitcnt lgkmcnt(7)
	s_waitcnt lgkmcnt(6)
	s_waitcnt lgkmcnt(5)
	v_mfma_f32_32x32x16_bf16 v[32:47], v[36:39], v[80:83], 0
	s_waitcnt lgkmcnt(4)
	s_waitcnt lgkmcnt(3)
	s_waitcnt lgkmcnt(2)
	s_waitcnt lgkmcnt(1)
	v_mfma_f32_32x32x16_bf16 v[32:47], v[66:69], v[84:87], v[32:47]
	s_waitcnt lgkmcnt(0)
	v_mfma_f32_32x32x16_bf16 v[32:47], v[70:73], v[88:91], v[32:47]
	v_mfma_f32_32x32x16_bf16 v[32:47], v[74:77], v[92:95], v[32:47]
	v_mfma_f32_32x32x16_bf16 v[48:63], v[158:161], v[92:95], v[48:63]
	s_cbranch_vccnz .LBB0_667
	s_nop 10
	v_pk_fma_f32 v[66:67], v[62:63], s[96:97], v[124:125] op_sel_hi:[1,0,1]
	v_pk_fma_f32 v[68:69], v[60:61], s[96:97], v[126:127] op_sel_hi:[1,0,1]
	v_pk_fma_f32 v[70:71], v[58:59], s[96:97], v[128:129] op_sel_hi:[1,0,1]
	v_pk_fma_f32 v[72:73], v[56:57], s[96:97], v[130:131] op_sel_hi:[1,0,1]
	v_pk_fma_f32 v[74:75], v[54:55], s[96:97], v[132:133] op_sel_hi:[1,0,1]
	v_pk_fma_f32 v[76:77], v[52:53], s[96:97], v[134:135] op_sel_hi:[1,0,1]
	v_pk_fma_f32 v[78:79], v[50:51], s[96:97], v[136:137] op_sel_hi:[1,0,1]
	v_pk_fma_f32 v[122:123], v[48:49], s[96:97], v[138:139] op_sel_hi:[1,0,1]
	s_mov_b64 s[18:19], 0
